# combine_norm (phase 10): slot row prefetched one row ahead so the expert-output loads no longer wait for the residual row
# speedup vs baseline: 1.0095x; 1.0018x over previous
.LBB0_1518:
	s_cmp_gt_i32 s50, 10
	s_cselect_b64 s[0:1], -1, 0
	s_cmp_lt_i32 s51, 11
	s_cselect_b64 s[2:3], -1, 0
	s_or_b64 s[0:1], s[0:1], s[2:3]
	v_mov_b32_e32 v1, v0
	s_and_b64 vcc, exec, s[0:1]
	s_cbranch_vccnz .LBB0_1555
	v_mov_b32_e32 v19, v0
	v_readlane_b32 s2, v253, 63
	v_ashrrev_i32_e32 v2, 6, v19
	s_nop 0
	v_add_u32_e32 v18, s2, v2
	s_movk_i32 s2, 0x4000
	v_cmp_gt_i32_e32 vcc, s2, v18
	s_and_saveexec_b64 s[2:3], vcc
	s_cbranch_execz .LBB0_1554
	v_and_b32_e32 v20, 63, v19
	v_readlane_b32 s4, v253, 2
	v_lshlrev_b32_e32 v14, 4, v20
	v_readlane_b32 s16, v253, 14
	v_readlane_b32 s17, v253, 15
	s_waitcnt lgkmcnt(0)
	s_nop 3
	global_load_dwordx4 v[2:5], v14, s[16:17]
	global_load_dwordx4 v[6:9], v14, s[16:17] offset:1024
	global_load_dwordx4 v[10:13], v14, s[16:17] offset:2048
	s_nop 0
	global_load_dwordx4 v[14:17], v14, s[16:17] offset:3072
	v_and_b32_e32 v24, 15, v19
	v_mbcnt_lo_u32_b32 v19, -1, 0
	v_mbcnt_hi_u32_b32 v19, -1, v19
	v_and_b32_e32 v21, 64, v19
	v_add_u32_e32 v21, 64, v21
	v_xor_b32_e32 v22, 32, v19
	v_cmp_lt_i32_e32 vcc, v22, v21
	v_readlane_b32 s6, v253, 4
	v_readlane_b32 s7, v253, 5
	v_cndmask_b32_e32 v22, v19, v22, vcc
	v_lshlrev_b32_e32 v44, 2, v22
	v_xor_b32_e32 v22, 16, v19
	v_cmp_lt_i32_e32 vcc, v22, v21
	v_readlane_b32 s6, v252, 13
	v_lshlrev_b32_e32 v26, 3, v20
	v_cndmask_b32_e32 v22, v19, v22, vcc
	v_lshlrev_b32_e32 v45, 2, v22
	v_xor_b32_e32 v22, 8, v19
	v_cmp_lt_i32_e32 vcc, v22, v21
	v_mov_b32_e32 v27, 0
	v_readlane_b32 s7, v252, 14
	v_cndmask_b32_e32 v22, v19, v22, vcc
	v_lshlrev_b32_e32 v46, 2, v22
	v_xor_b32_e32 v22, 4, v19
	v_cmp_lt_i32_e32 vcc, v22, v21
	v_readlane_b32 s8, v253, 6
	v_readlane_b32 s5, v253, 3
	v_cndmask_b32_e32 v22, v19, v22, vcc
	v_lshlrev_b32_e32 v47, 2, v22
	v_xor_b32_e32 v22, 2, v19
	v_cmp_lt_i32_e32 vcc, v22, v21
	v_readlane_b32 s9, v253, 7
	v_readlane_b32 s10, v253, 8
	v_cndmask_b32_e32 v22, v19, v22, vcc
	v_lshlrev_b32_e32 v48, 2, v22
	v_xor_b32_e32 v22, 1, v19
	v_cmp_lt_i32_e32 vcc, v22, v21
	v_lshl_add_u64 v[20:21], s[6:7], 0, v[26:27]
	s_mov_b64 s[6:7], 0x700000
	v_cndmask_b32_e32 v19, v19, v22, vcc
	v_lshlrev_b32_e32 v49, 2, v19
	v_ashrrev_i32_e32 v19, 31, v18
	v_lshlrev_b64 v[22:23], 6, v[18:19]
	v_lshl_or_b32 v22, v24, 2, v22
	v_lshl_add_u64 v[22:23], v[22:23], 0, s[6:7]
	v_readlane_b32 s6, v252, 0
	s_mov_b32 s8, s6
	v_readlane_b32 s11, v253, 9
	v_readlane_b32 s12, v253, 10
	v_readlane_b32 s13, v253, 11
	v_readlane_b32 s14, v253, 12
	v_readlane_b32 s15, v253, 13
	v_readlane_b32 s18, v253, 16
	v_readlane_b32 s19, v253, 17
	s_mov_b32 s5, 0
	v_readlane_b32 s7, v252, 1
	s_ashr_i32 s9, s6, 31
	v_lshlrev_b64 v[24:25], 11, v[18:19]
	s_mov_b32 s4, s8
	s_lshl_b64 s[6:7], s[8:9], 6
	v_or_b32_e32 v24, v24, v26
	v_writelane_b32 v252, s4, 0
	s_lshl_b64 s[8:9], s[8:9], 11
	s_mov_b64 s[10:11], 0
	s_mov_b64 s[12:13], 0x800000
	s_mov_b32 s20, 0x800000
	s_mov_b64 s[14:15], 0x800200
	s_mov_b64 s[16:17], 0x800400
	s_mov_b64 s[18:19], 0x800600
	v_mov_b32_e32 v19, 0x358637bd
	s_mov_b32 s21, 0x4800000
	s_movk_i32 s22, 0x3fff
	v_writelane_b32 v252, s5, 1
	v_lshl_add_u64 v[202:203], s[48:49], 0, v[22:23]
	global_load_dword v204, v[202:203], off
	s_waitcnt vmcnt(0)
	s_branch .LBB0_1522

.LBB0_1522:
	v_lshl_add_u64 v[26:27], s[48:49], 0, v[24:25]
	v_add_co_u32_e32 v28, vcc, 0x800000, v26
	v_lshl_add_u64 v[30:31], s[48:49], 0, v[22:23]
	v_lshl_add_u64 v[202:203], v[30:31], 0, s[6:7]
	v_mov_b32_e32 v50, v204
	global_load_dword v204, v[202:203], off
	v_addc_co_u32_e32 v29, vcc, 0, v27, vcc
	global_load_dwordx2 v[30:31], v[28:29], off
	global_load_dwordx2 v[32:33], v[28:29], off offset:512
	global_load_dwordx2 v[52:53], v[28:29], off offset:1024
	s_nop 0
	global_load_dwordx2 v[28:29], v[28:29], off offset:1536
	v_readlane_b32 s4, v50, 0
	s_cmp_lt_i32 s4, 0
	s_cbranch_scc1 .Lcna_0
	s_lshl_b64 s[24:25], s[4:5], 11
	v_lshl_add_u64 v[200:201], v[20:21], 0, s[24:25]
	global_load_dwordx2 v[72:73], v[200:201], off
	global_load_dwordx2 v[74:75], v[200:201], off offset:512
	global_load_dwordx2 v[76:77], v[200:201], off offset:1024
	global_load_dwordx2 v[78:79], v[200:201], off offset:1536
